# baseline (speedup 1.0000x reference)
_Z16sum_layer_kernelPKfS0_Pf:
	s_load_dwordx4 s[4:7], s[0:1], 0x0
	s_load_dwordx2 s[8:9], s[0:1], 0x10
	v_and_b32_e32 v40, 31, v0
	v_bfe_u32 v41, v0, 5, 1
	v_lshrrev_b32_e32 v42, 6, v0
	v_and_b32_e32 v43, 7, v0
	v_bfe_u32 v44, v0, 3, 3
	v_and_b32_e32 v45, 63, v0
	s_lshl_b32 s3, s2, 12
	s_lshl_b32 s19, s2, 7
	v_lshlrev_b32_e32 v1, 11, v41
	v_lshl_or_b32 v1, v40, 2, v1
	v_lshlrev_b32_e32 v46, 4, v43
	v_lshl_add_u32 v35, v44, 16, v46
	v_lshl_add_u32 v35, v42, 21, v35
	v_add_u32_e32 v35, s19, v35
	v_lshlrev_b32_e32 v36, 2, v40
	v_lshl_add_u32 v36, v41, 18, v36
	v_lshl_add_u32 v36, v42, 21, v36
	v_add_u32_e32 v36, s19, v36
	v_mul_u32_u24_e32 v37, 0x1200, v42
	v_mul_u32_u24_e32 v38, 0x90, v44
	v_add3_u32 v38, v37, v38, v46
	v_mul_u32_u24_e32 v39, 0x90, v40
	v_lshlrev_b32_e32 v47, 6, v41
	v_add3_u32 v39, v37, v39, v47
	v_cmp_gt_u32_e32 vcc, 32, v45
	v_mov_b32_e32 v34, 0xc1600000
	s_mov_b32 s16, 0x3fb8aa3b
	s_mov_b32 s17, 0x3f317218
	s_mov_b32 s20, 0x80000
	s_mov_b32 s21, 0x100000
	s_mov_b32 s22, 0x180000
	s_lshl_b32 s24, 1, 16
	s_lshl_b32 s25, 2, 16
	s_lshl_b32 s26, 3, 16
	s_lshl_b32 s27, 8, 16
	s_lshl_b32 s28, 9, 16
	s_lshl_b32 s29, 10, 16
	s_lshl_b32 s30, 11, 16
	s_lshl_b32 s31, 16, 16
	s_lshl_b32 s32, 17, 16
	s_lshl_b32 s33, 18, 16
	s_lshl_b32 s34, 19, 16
	s_lshl_b32 s35, 24, 16
	s_lshl_b32 s36, 25, 16
	s_lshl_b32 s37, 26, 16
	s_lshl_b32 s38, 27, 16
	s_mov_b32 s14, 0x200000
	s_mov_b32 s15, 0x20000
	s_waitcnt lgkmcnt(0)
	s_mov_b32 s12, s6
	s_and_b32 s13, s7, 0xffff
	s_and_b32 s5, s5, 0xffff
	s_mov_b32 s6, 0x800000
	s_mov_b32 s7, s15
	s_and_b32 s9, s9, 0xffff
	s_mov_b32 s10, s6
	s_mov_b32 s11, s15
	buffer_load_dword v18, v1, s[12:15], s3 offen nt
	buffer_load_dword v19, v1, s[12:15], s3 offen offset:128 nt
	buffer_load_dword v20, v1, s[12:15], s3 offen offset:256 nt
	buffer_load_dword v21, v1, s[12:15], s3 offen offset:384 nt
	buffer_load_dword v22, v1, s[12:15], s3 offen offset:512 nt
	buffer_load_dword v23, v1, s[12:15], s3 offen offset:640 nt
	buffer_load_dword v24, v1, s[12:15], s3 offen offset:768 nt
	buffer_load_dword v25, v1, s[12:15], s3 offen offset:896 nt
	buffer_load_dword v26, v1, s[12:15], s3 offen offset:1024 nt
	buffer_load_dword v27, v1, s[12:15], s3 offen offset:1152 nt
	buffer_load_dword v28, v1, s[12:15], s3 offen offset:1280 nt
	buffer_load_dword v29, v1, s[12:15], s3 offen offset:1408 nt
	buffer_load_dword v30, v1, s[12:15], s3 offen offset:1536 nt
	buffer_load_dword v31, v1, s[12:15], s3 offen offset:1664 nt
	buffer_load_dword v32, v1, s[12:15], s3 offen offset:1792 nt
	buffer_load_dword v33, v1, s[12:15], s3 offen offset:1920 nt
	buffer_load_dwordx4 v[2:5], v35, s[4:7], 0 offen nt
	buffer_load_dwordx4 v[6:9], v35, s[4:7], s20 offen nt
	buffer_load_dwordx4 v[10:13], v35, s[4:7], s21 offen nt
	buffer_load_dwordx4 v[14:17], v35, s[4:7], s22 offen nt
	s_waitcnt vmcnt(4)
	v_max3_f32 v49, v18, v19, v20
	v_max3_f32 v50, v21, v22, v23
	v_max3_f32 v49, v49, v24, v25
	v_max3_f32 v50, v50, v26, v27
	v_max3_f32 v49, v49, v28, v29
	v_max3_f32 v50, v50, v30, v31
	v_max3_f32 v49, v49, v32, v33
	v_max_f32_e32 v49, v49, v50
	v_mov_b32_e32 v50, v49
	s_nop 1
	v_permlane32_swap_b32_e32 v49, v50
	v_max_f32_e32 v49, v49, v50
	v_fmamk_f32 v49, v49, 0x3fb8aa3b, v34
	v_fma_f32 v18, v18, s16, -v49
	v_exp_f32_e32 v18, v18
	v_fma_f32 v19, v19, s16, -v49
	v_exp_f32_e32 v19, v19
	v_fma_f32 v20, v20, s16, -v49
	v_exp_f32_e32 v20, v20
	v_fma_f32 v21, v21, s16, -v49
	v_exp_f32_e32 v21, v21
	v_fma_f32 v22, v22, s16, -v49
	v_exp_f32_e32 v22, v22
	v_fma_f32 v23, v23, s16, -v49
	v_exp_f32_e32 v23, v23
	v_fma_f32 v24, v24, s16, -v49
	v_exp_f32_e32 v24, v24
	v_fma_f32 v25, v25, s16, -v49
	v_exp_f32_e32 v25, v25
	v_fma_f32 v26, v26, s16, -v49
	v_exp_f32_e32 v26, v26
	v_fma_f32 v27, v27, s16, -v49
	v_exp_f32_e32 v27, v27
	v_fma_f32 v28, v28, s16, -v49
	v_exp_f32_e32 v28, v28
	v_fma_f32 v29, v29, s16, -v49
	v_exp_f32_e32 v29, v29
	v_fma_f32 v30, v30, s16, -v49
	v_exp_f32_e32 v30, v30
	v_fma_f32 v31, v31, s16, -v49
	v_exp_f32_e32 v31, v31
	v_fma_f32 v32, v32, s16, -v49
	v_exp_f32_e32 v32, v32
	v_fma_f32 v33, v33, s16, -v49
	v_exp_f32_e32 v33, v33
	v_add_f32_e32 v50, v18, v19
	v_add_f32_e32 v51, v20, v21
	v_add_f32_e32 v50, v50, v22
	v_add_f32_e32 v51, v51, v23
	v_add_f32_e32 v50, v50, v24
	v_add_f32_e32 v51, v51, v25
	v_add_f32_e32 v50, v50, v26
	v_add_f32_e32 v51, v51, v27
	v_add_f32_e32 v50, v50, v28
	v_add_f32_e32 v51, v51, v29
	v_add_f32_e32 v50, v50, v30
	v_add_f32_e32 v51, v51, v31
	v_add_f32_e32 v50, v50, v32
	v_add_f32_e32 v51, v51, v33
	v_add_f32_e32 v50, v50, v51
	v_mov_b32_e32 v51, v50
	s_nop 1
	v_permlane32_swap_b32_e32 v50, v51
	v_add_f32_e32 v50, v50, v51
	v_log_f32_e32 v50, v50
	v_cvt_pk_f16_f32 v40, v18, v19
	v_cvt_pk_f16_f32 v41, v20, v21
	v_cvt_pk_f16_f32 v42, v22, v23
	v_cvt_pk_f16_f32 v43, v24, v25
	v_cvt_pk_f16_f32 v44, v26, v27
	v_cvt_pk_f16_f32 v45, v28, v29
	v_cvt_pk_f16_f32 v46, v30, v31
	v_cvt_pk_f16_f32 v47, v32, v33
	v_add_f32_e32 v50, 0x41600000, v50
	v_mul_f32_e32 v50, 0xbf317218, v50
	v_cndmask_b32_e64 v51, v50, 1.0, vcc
	s_waitcnt vmcnt(3)
	ds_write_b128 v38, v[2:5]
	s_waitcnt vmcnt(2)
	ds_write_b128 v38, v[6:9] offset:1152
	s_waitcnt vmcnt(1)
	ds_write_b128 v38, v[10:13] offset:2304
	s_waitcnt vmcnt(0)
	ds_write_b128 v38, v[14:17] offset:3456
	ds_read_b128 v[2:5], v39
	ds_read_b128 v[6:9], v39 offset:16
	ds_read_b128 v[10:13], v39 offset:32
	ds_read_b128 v[14:17], v39 offset:48
	s_waitcnt lgkmcnt(2)
	v_max3_f32 v52, v2, v3, v4
	v_max3_f32 v53, v5, v6, v7
	v_max_f32_e32 v52, v52, v8
	v_max_f32_e32 v53, v53, v9
	s_waitcnt lgkmcnt(0)
	v_max3_f32 v52, v52, v10, v11
	v_max3_f32 v53, v53, v12, v13
	v_max3_f32 v52, v52, v14, v15
	v_max3_f32 v53, v53, v16, v17
	v_max_f32_e32 v52, v52, v53
	v_mov_b32_e32 v53, v52
	s_nop 1
	v_permlane32_swap_b32_e32 v52, v53
	v_max_f32_e32 v52, v52, v53
	v_cndmask_b32_e32 v54, 1.0, v52, vcc
	v_fmamk_f32 v55, v52, 0x3fb8aa3b, v34
	v_fma_f32 v2, v2, s16, -v55
	v_mfma_f32_32x32x2_f32 v[64:79], v54, v51, 0
	v_exp_f32_e32 v2, v2
	v_fma_f32 v3, v3, s16, -v55
	v_exp_f32_e32 v3, v3
	v_fma_f32 v4, v4, s16, -v55
	v_exp_f32_e32 v4, v4
	v_fma_f32 v5, v5, s16, -v55
	v_exp_f32_e32 v5, v5
	v_fma_f32 v6, v6, s16, -v55
	v_exp_f32_e32 v6, v6
	v_fma_f32 v7, v7, s16, -v55
	v_exp_f32_e32 v7, v7
	v_fma_f32 v8, v8, s16, -v55
	v_exp_f32_e32 v8, v8
	v_fma_f32 v9, v9, s16, -v55
	v_exp_f32_e32 v9, v9
	v_fma_f32 v10, v10, s16, -v55
	v_exp_f32_e32 v10, v10
	v_cvt_pk_f16_f32 v56, v2, v3
	v_cvt_pk_f16_f32 v57, v4, v5
	v_cvt_pk_f16_f32 v58, v6, v7
	v_cvt_pk_f16_f32 v59, v8, v9
	v_fma_f32 v11, v11, s16, -v55
	v_exp_f32_e32 v11, v11
	v_fma_f32 v12, v12, s16, -v55
	v_exp_f32_e32 v12, v12
	v_mfma_f32_32x32x16_f16 v[18:33], v[56:59], v[40:43], 0
	v_fma_f32 v13, v13, s16, -v55
	v_exp_f32_e32 v13, v13
	v_fma_f32 v14, v14, s16, -v55
	v_exp_f32_e32 v14, v14
	v_fma_f32 v15, v15, s16, -v55
	v_exp_f32_e32 v15, v15
	v_fma_f32 v16, v16, s16, -v55
	v_exp_f32_e32 v16, v16
	v_fma_f32 v17, v17, s16, -v55
	v_exp_f32_e32 v17, v17
	v_cvt_pk_f16_f32 v60, v10, v11
	v_cvt_pk_f16_f32 v61, v12, v13
	v_cvt_pk_f16_f32 v62, v14, v15
	v_cvt_pk_f16_f32 v63, v16, v17
	s_nop 1
	v_mfma_f32_32x32x16_f16 v[18:33], v[60:63], v[44:47], v[18:33]
	ds_read_b128 v[2:5], v39
	ds_read_b128 v[6:9], v39 offset:16
	ds_read_b128 v[10:13], v39 offset:32
	ds_read_b128 v[14:17], v39 offset:48
	s_waitcnt lgkmcnt(2)
	v_max3_f32 v52, v2, v3, v4
	v_max3_f32 v53, v5, v6, v7
	v_max_f32_e32 v52, v52, v8
	v_max_f32_e32 v53, v53, v9
	s_waitcnt lgkmcnt(0)
	v_max3_f32 v52, v52, v10, v11
	v_max3_f32 v53, v53, v12, v13
	v_max3_f32 v52, v52, v14, v15
	v_max3_f32 v53, v53, v16, v17
	v_max_f32_e32 v52, v52, v53
	v_mov_b32_e32 v53, v52
	s_nop 1
	v_permlane32_swap_b32_e32 v52, v53
	v_max_f32_e32 v52, v52, v53
	v_cndmask_b32_e32 v54, 1.0, v52, vcc
	v_fmamk_f32 v55, v52, 0x3fb8aa3b, v34
	v_fma_f32 v2, v2, s16, -v55
	v_mfma_f32_32x32x2_f32 v[64:79], v54, v51, 0
	v_exp_f32_e32 v2, v2
	v_fma_f32 v3, v3, s16, -v55
	v_exp_f32_e32 v3, v3
	v_fma_f32 v4, v4, s16, -v55
	v_exp_f32_e32 v4, v4
	v_fma_f32 v5, v5, s16, -v55
	v_exp_f32_e32 v5, v5
	v_fma_f32 v6, v6, s16, -v55
	v_exp_f32_e32 v6, v6
	v_fma_f32 v7, v7, s16, -v55
	v_exp_f32_e32 v7, v7
	v_fma_f32 v8, v8, s16, -v55
	v_exp_f32_e32 v8, v8
	v_fma_f32 v9, v9, s16, -v55
	v_exp_f32_e32 v9, v9
	v_fma_f32 v10, v10, s16, -v55
	v_exp_f32_e32 v10, v10
	v_cvt_pk_f16_f32 v56, v2, v3
	v_cvt_pk_f16_f32 v57, v4, v5
	v_cvt_pk_f16_f32 v58, v6, v7
	v_cvt_pk_f16_f32 v59, v8, v9
	v_fma_f32 v11, v11, s16, -v55
	v_exp_f32_e32 v11, v11
	v_fma_f32 v12, v12, s16, -v55
	v_exp_f32_e32 v12, v12
	v_mfma_f32_32x32x16_f16 v[18:33], v[56:59], v[40:43], 0
	v_fma_f32 v13, v13, s16, -v55
	v_exp_f32_e32 v13, v13
	v_fma_f32 v14, v14, s16, -v55
	v_exp_f32_e32 v14, v14
	v_fma_f32 v15, v15, s16, -v55
	v_exp_f32_e32 v15, v15
	v_fma_f32 v16, v16, s16, -v55
	v_exp_f32_e32 v16, v16
	v_fma_f32 v17, v17, s16, -v55
	v_exp_f32_e32 v17, v17
	v_cvt_pk_f16_f32 v60, v10, v11
	v_cvt_pk_f16_f32 v61, v12, v13
	v_cvt_pk_f16_f32 v62, v14, v15
	v_cvt_pk_f16_f32 v63, v16, v17
	s_nop 1
	v_mfma_f32_32x32x16_f16 v[18:33], v[60:63], v[44:47], v[18:33]
	s_nop 11
	v_log_f32_e32 v18, v18
	v_log_f32_e32 v19, v19
	v_log_f32_e32 v20, v20
	v_fmac_f32_e32 v64, s17, v18
	buffer_store_dword v64, v36, s[8:11], 0 offen
	v_log_f32_e32 v21, v21
	v_fmac_f32_e32 v65, s17, v19
	buffer_store_dword v65, v36, s[8:11], s24 offen
	v_log_f32_e32 v22, v22
	v_fmac_f32_e32 v66, s17, v20
	buffer_store_dword v66, v36, s[8:11], s25 offen
	v_log_f32_e32 v23, v23
	v_fmac_f32_e32 v67, s17, v21
	buffer_store_dword v67, v36, s[8:11], s26 offen
	v_log_f32_e32 v24, v24
	v_fmac_f32_e32 v68, s17, v22
	buffer_store_dword v68, v36, s[8:11], s27 offen
	v_log_f32_e32 v25, v25
	v_fmac_f32_e32 v69, s17, v23
	buffer_store_dword v69, v36, s[8:11], s28 offen
	v_log_f32_e32 v26, v26
	v_fmac_f32_e32 v70, s17, v24
	buffer_store_dword v70, v36, s[8:11], s29 offen
	v_log_f32_e32 v27, v27
	v_fmac_f32_e32 v71, s17, v25
	buffer_store_dword v71, v36, s[8:11], s30 offen
	v_log_f32_e32 v28, v28
	v_fmac_f32_e32 v72, s17, v26
	buffer_store_dword v72, v36, s[8:11], s31 offen
	v_log_f32_e32 v29, v29
	v_fmac_f32_e32 v73, s17, v27
	buffer_store_dword v73, v36, s[8:11], s32 offen
	v_log_f32_e32 v30, v30
	v_fmac_f32_e32 v74, s17, v28
	buffer_store_dword v74, v36, s[8:11], s33 offen
	v_log_f32_e32 v31, v31
	v_fmac_f32_e32 v75, s17, v29
	buffer_store_dword v75, v36, s[8:11], s34 offen
	v_log_f32_e32 v32, v32
	v_fmac_f32_e32 v76, s17, v30
	buffer_store_dword v76, v36, s[8:11], s35 offen
	v_log_f32_e32 v33, v33
	v_fmac_f32_e32 v77, s17, v31
	buffer_store_dword v77, v36, s[8:11], s36 offen
	v_fmac_f32_e32 v78, s17, v32
	buffer_store_dword v78, v36, s[8:11], s37 offen
	v_fmac_f32_e32 v79, s17, v33
	buffer_store_dword v79, v36, s[8:11], s38 offen
	s_endpgm
